# baseline (speedup 1.0000x reference)
.LBB6_39:
	v_lshlrev_b32_e32 v2, 3, v114
	s_lshl_b32 s0, s38, 9
	v_and_or_b32 v2, v2, 64, s0
	v_or_b32_e32 v2, s39, v2
	v_or_b32_e32 v6, s33, v2
	v_lshrrev_b32_e32 v7, 4, v0
	v_lshlrev_b32_e32 v1, 4, v114
	v_lshl_or_b32 v16, v6, 6, v7
	v_and_b32_e32 v2, 0x70, v1
	v_mov_b32_e32 v3, 0
	s_movk_i32 s0, 0x110
	v_or_b32_e32 v12, s27, v16
	s_waitcnt lgkmcnt(0)
	v_lshl_add_u64 v[10:11], s[28:29], 0, v[2:3]
	v_mad_u32_u24 v2, v7, s0, v1
	v_ashrrev_i32_e32 v13, 31, v12
	s_waitcnt vmcnt(0)
	s_barrier
	ds_read_b128 v[20:23], v2
	v_or_b32_e32 v6, 0x200, v0
	v_lshrrev_b32_e32 v6, 4, v6
	v_mad_u32_u24 v6, v6, s0, v1
	ds_read_b128 v[24:27], v6
	v_or_b32_e32 v6, 0x400, v0
	v_lshrrev_b32_e32 v6, 4, v6
	v_mad_u32_u24 v6, v6, s0, v1
	ds_read_b128 v[28:31], v6
	v_or_b32_e32 v6, 0x600, v0
	v_lshrrev_b32_e32 v6, 4, v6
	v_mad_u32_u24 v6, v6, s0, v1
	ds_read_b128 v[32:35], v6
	v_or_b32_e32 v6, 0x800, v0
	v_lshrrev_b32_e32 v6, 4, v6
	v_mad_u32_u24 v6, v6, s0, v1
	ds_read_b128 v[36:39], v6
	v_or_b32_e32 v6, 0xa00, v0
	v_lshrrev_b32_e32 v6, 4, v6
	v_mad_u32_u24 v6, v6, s0, v1
	ds_read_b128 v[40:43], v6
	v_or_b32_e32 v6, 0xc00, v0
	v_lshrrev_b32_e32 v6, 4, v6
	v_mad_u32_u24 v6, v6, s0, v1
	ds_read_b128 v[44:47], v6
	v_or_b32_e32 v6, 0xe00, v0
	v_lshrrev_b32_e32 v6, 4, v6
	v_mad_u32_u24 v6, v6, s0, v1
	ds_read_b128 v[48:51], v6
	v_lshlrev_b64 v[6:7], 7, v[12:13]
	v_lshl_add_u64 v[52:53], v[10:11], 0, v[6:7]
	v_or_b32_e32 v6, 0x40, v12
	v_ashrrev_i32_e32 v7, 31, v6
	v_lshlrev_b64 v[6:7], 7, v[6:7]
	v_lshl_add_u64 v[54:55], v[10:11], 0, v[6:7]
	v_or_b32_e32 v6, 0x80, v12
	v_ashrrev_i32_e32 v7, 31, v6
	v_lshlrev_b64 v[6:7], 7, v[6:7]
	v_lshl_add_u64 v[56:57], v[10:11], 0, v[6:7]
	v_or_b32_e32 v6, 0xc0, v12
	v_ashrrev_i32_e32 v7, 31, v6
	v_lshlrev_b64 v[6:7], 7, v[6:7]
	v_lshl_add_u64 v[58:59], v[10:11], 0, v[6:7]
	v_or_b32_e32 v6, 0x100, v12
	v_ashrrev_i32_e32 v7, 31, v6
	v_lshlrev_b64 v[6:7], 7, v[6:7]
	v_lshl_add_u64 v[60:61], v[10:11], 0, v[6:7]
	v_or_b32_e32 v6, 0x140, v12
	v_ashrrev_i32_e32 v7, 31, v6
	v_lshlrev_b64 v[6:7], 7, v[6:7]
	v_lshl_add_u64 v[62:63], v[10:11], 0, v[6:7]
	v_or_b32_e32 v6, 0x180, v12
	v_ashrrev_i32_e32 v7, 31, v6
	v_lshlrev_b64 v[6:7], 7, v[6:7]
	v_lshl_add_u64 v[64:65], v[10:11], 0, v[6:7]
	v_add_u32_e32 v6, 0x1c0, v16
	v_or_b32_e32 v6, s27, v6
	v_ashrrev_i32_e32 v7, 31, v6
	v_lshlrev_b64 v[6:7], 7, v[6:7]
	v_lshl_add_u64 v[66:67], v[10:11], 0, v[6:7]
	s_waitcnt lgkmcnt(7)
	global_store_dwordx4 v[52:53], v[20:23], off nt
	s_waitcnt lgkmcnt(6)
	global_store_dwordx4 v[54:55], v[24:27], off nt
	s_waitcnt lgkmcnt(5)
	global_store_dwordx4 v[56:57], v[28:31], off nt
	s_waitcnt lgkmcnt(4)
	global_store_dwordx4 v[58:59], v[32:35], off nt
	s_waitcnt lgkmcnt(3)
	global_store_dwordx4 v[60:61], v[36:39], off nt
	s_waitcnt lgkmcnt(2)
	global_store_dwordx4 v[62:63], v[40:43], off nt
	s_waitcnt lgkmcnt(1)
	global_store_dwordx4 v[64:65], v[44:47], off nt
	s_waitcnt lgkmcnt(0)
	global_store_dwordx4 v[66:67], v[48:51], off nt
	s_endpgm
	.p2align	8
